# MoBA tile loop: one barrier per three steps, the next triple's three tiles requested together at the first step of a triple
# baseline (speedup 1.0000x reference)
; #define ATT_WAIT_BAR(N) asm volatile("s_waitcnt vmcnt(" #N ") lgkmcnt(0)\n\ts_barrier" ::: "memory")
; template <class BIAS>
; __device__ __forceinline__ void attn_tiles(char* shm, const UnitIO& io, int t_begin, int t_end, const BIAS& B, int tid) {
;     const int lane = tid & 63, r32 = lane & 31, hi = lane >> 5; const int wid = __builtin_amdgcn_readfirstlane(tid >> 6);
;     const unsigned lds0 = (unsigned)(uintptr_t)shm;
;     const bf16* ksrc = io.K0 + (long)lane * io.kstride + wid * 8;
;     const bf16* vsrc = io.V0 + (long)(16 * (wid & 3) + (lane >> 2)) * io.kstride + (wid >> 2) * 32 + (lane & 3) * 8;
;     const unsigned kdst = lds0 + LDS_K + wid * 1024, vdst = lds0 + LDS_V + wid * 1024;
;     const long tstep = 64 * io.kstride;
;     ...
;     const lds_cptr shm3 = (lds_cptr)shm;
;     const lds_cptr kp0 = shm3 + LDS_K + hi * 1024 + r32 * 16;
;     const lds_cptr vp0 = shm3 + LDS_V + ((lane >> 4) & 1) * 32 + (lane & 3) * 8 + (4 * hi + ((lane & 15) >> 2)) * 64;
;     float* wsf = (float*)(shm + LDS_WS) + wid * 64;
;     bf16x8 qr[4];
;     { const bf16* qp = io.Q + (long)r32 * io.qstride + hi * 8;
; #pragma unroll
;       for (int d0 = 0; d0 < 4; ++d0) qr[d0] = *reinterpret_cast<const bf16x8*>(qp + d0 * 16); }
;     ATT_DMA(t_begin, 0);
;     asm volatile("" :: "v"(qr[0]), "v"(qr[1]), "v"(qr[2]), "v"(qr[3]));
;     const int nt_ = t_end - t_begin; if (nt_ > 1) ATT_DMA(t_begin + 1, SLOTB); if (nt_ > 2) ATT_DMA(t_begin + 2, 2 * SLOTB);
;     f32x16 o[2]; o[0] = f32x16{}; o[1] = f32x16{}; float l_reg = 0.f;
;     if (nt_ > 2) ATT_WAIT_BAR(4); else if (nt_ > 1) ATT_WAIT_BAR(2); else ATT_WAIT_BAR(0);
; __device__ __forceinline__ void moba_unit(Frame& F, const AttnBufs& A, int b, int h, int qb) {
;     ...
;     unsigned selmask = 0u; if (i0 >= 0) selmask |= 1u << i0; if (i1 >= 0) selmask |= 1u << i1; if (i2 >= 0) selmask |= 1u << i2;
;     att::BiasMoba B; B.slope2 = exp2f(-8.0f * (float)(7 + h) / 10.0f) * LOG2E; B.qrel = w * 32 + r32; B.tqf = (float)(qb * 256 + B.qrel); B.hi = hi; B.w = w; B.nb0 = 4 * qb; B.selmask = selmask; B.u = 32 * (w & 1) + r32 - 4 * hi;
;     att::UnitIO io; io.Q = Qw; io.qstride = DM; io.K0 = A.K + bo + (size_t)b * SEQ * DM + h * 64; io.V0 = A.V + bo + (size_t)b * SEQ * DM + h * 64; io.kstride = DM;
;     io.O = A.O + bo + row0 * DM + h * 64; io.ostride = DM; io.L = nullptr; io.lstride = 0; io.norm = true;
.LBB0_294:
	v_lshlrev_b32_e64 v2, v41, 1
	v_cmp_lt_i32_e32 vcc, -1, v41
	v_lshlrev_b32_e64 v3, v5, 1
	v_lshlrev_b32_e32 v148, 1, v154
	v_cndmask_b32_e32 v2, 0, v2, vcc
	v_cmp_lt_i32_e32 vcc, -1, v5
	v_lshlrev_b32_e64 v5, v4, 1
	v_mov_b32_e32 v149, v1
	v_cndmask_b32_e32 v3, 0, v3, vcc
	v_cmp_lt_i32_e32 vcc, -1, v4
	v_readfirstlane_b32 s27, v232
	s_ashr_i32 s16, s27, 6
	v_cndmask_b32_e32 v4, 0, v5, vcc
	v_or3_b32 v135, v3, v2, v4
	v_add_u32_e32 v2, s22, v143
	v_cvt_f32_i32_e32 v137, v2
	v_lshl_add_u64 v[2:3], s[4:5], 0, v[132:133]
	v_lshl_add_u64 v[2:3], v[2:3], 0, v[148:149]
	s_lshl_b32 s12, s16, 4
	v_and_or_b32 v4, s12, 48, v178
	s_ashr_i32 s12, s27, 3
	s_lshl_b32 s14, s16, 3
	s_andn2_b32 s12, s12, 31
	s_ashr_i32 s15, s14, 31
	s_ashr_i32 s13, s12, 31
	v_lshlrev_b32_e32 v4, 11, v4
	v_mov_b32_e32 v5, v1
	s_lshl_b64 s[4:5], s[14:15], 1
	v_lshl_add_u64 v[4:5], s[30:31], 0, v[4:5]
	s_lshl_b64 s[12:13], s[12:13], 1
	s_lshl_b32 s29, s16, 10
	v_lshl_add_u64 v[2:3], v[156:157], 0, s[4:5]
	v_lshl_add_u64 v[2:3], v[2:3], 0, v[244:245]
	v_lshl_add_u64 v[4:5], v[4:5], 0, s[12:13]
	v_lshlrev_b32_e32 v150, 1, v144
	v_mov_b32_e32 v151, v1
	s_add_i32 s33, s29, 0x8000
	v_lshl_add_u64 v[4:5], v[4:5], 0, v[150:151]
	s_mov_b64 s[22:23], 0x20000
	s_add_i32 s14, s29, 0x2000
	v_lshl_add_u64 v[6:7], v[2:3], 0, s[22:23]
	v_mov_b32_e32 v16, v1
	v_mov_b32_e32 v17, v1
	s_lshl_b32 s26, s20, 2
	v_mov_b32_e32 v8, v1
	v_mov_b32_e32 v9, v1
	v_mov_b32_e32 v10, v1
	v_mov_b32_e32 v11, v1
	v_mov_b32_e32 v12, v1
	v_mov_b32_e32 v13, v1
	v_mov_b32_e32 v14, v1
	v_mov_b32_e32 v15, v1
	s_lshl_b64 s[10:11], s[10:11], 10
	s_mov_b32 s17, 0
	s_add_i32 s28, s26, 4
	v_lshl_add_u64 v[172:173], v[166:167], 0, s[4:5]
	v_lshl_add_u64 v[172:173], v[172:173], 0, v[244:245]
	s_sub_i32 s20, 0, s26
	s_sub_i32 s24, s72, s26
	v_mov_b32_e32 v139, 0
	v_mov_b32_e32 v149, v145
	s_add_i32 s14, s33, 0x2000
	v_lshl_add_u64 v[6:7], v[4:5], 0, s[22:23]
	s_mov_b64 s[22:23], 0x40000
	s_add_i32 s14, s29, 0x4000
	v_lshl_add_u64 v[2:3], v[2:3], 0, s[22:23]
	s_add_i32 s14, s33, 0x4000
	v_lshl_add_u64 v[2:3], v[4:5], 0, s[22:23]
	s_lshl_b32 s14, s16, 15
	s_and_b32 s14, s14, 0x18000
	v_lshl_or_b32 v2, v175, 1, s14
	v_mov_b32_e32 v3, v1
	s_waitcnt vmcnt(0) lgkmcnt(0)
	s_barrier
	v_lshl_add_u64 v[2:3], s[12:13], 0, v[2:3]
	v_lshl_add_u64 v[152:153], v[164:165], 0, v[2:3]
	v_mov_b32_e32 v2, v1
	v_mov_b32_e32 v3, v1
	v_mov_b32_e32 v4, v1
	v_mov_b32_e32 v5, v1
	v_mov_b32_e32 v6, v1
	v_mov_b32_e32 v7, v1
	v_mov_b64_e32 v[32:33], v[16:17]
	s_mov_b32 s22, 0
	v_mov_b64_e32 v[30:31], v[14:15]
	v_mov_b64_e32 v[28:29], v[12:13]
	v_mov_b64_e32 v[26:27], v[10:11]
	v_mov_b64_e32 v[24:25], v[8:9]
	v_mov_b64_e32 v[22:23], v[6:7]
	v_mov_b64_e32 v[20:21], v[4:5]
	v_mov_b64_e32 v[18:19], v[2:3]
	s_branch .LBB0_296

; #define ATT_DMA(t, slot) do { glds16(ksrc + (long)(t) * tstep, (unsigned)__builtin_amdgcn_readfirstlane(kdst + (slot))); glds16(vsrc + (long)(t) * tstep, (unsigned)__builtin_amdgcn_readfirstlane(vdst + (slot))); } while (0)
; template <class BIAS>
; __device__ __forceinline__ void attn_tiles(char* shm, const UnitIO& io, int t_begin, int t_end, const BIAS& B, int tid) {
;     ...
;     for (int t = t_begin; t < t_end; ++t) {
;         const int rem = t_end - t;
;         const bool act = B.active(t);
;         const int sl_c = ((t - t_begin) & 3) * SLOTB;
;         if (rem > 3) ATT_DMA(t + 3, ((t + 3 - t_begin) & 3) * SLOTB);
;         u32x4 pw[4]; f32x16 c1x;
.LBB0_296:
	s_cmp_lt_u32 s28, 4
	s_cselect_b64 s[12:13], -1, 0
	s_cmp_eq_u32 s22, 0
	s_cselect_b64 s[14:15], -1, 0
	s_cmp_eq_u32 s22, 3
	s_cselect_b64 s[100:101], -1, 0
	s_or_b64 s[14:15], s[14:15], s[100:101]
	s_orn2_b64 s[12:13], s[12:13], s[14:15]

; #define ATT_SBAR() __builtin_amdgcn_sched_barrier(0)
; #define ATT_DMA(t, slot) do { glds16(ksrc + (long)(t) * tstep, (unsigned)__builtin_amdgcn_readfirstlane(kdst + (slot))); glds16(vsrc + (long)(t) * tstep, (unsigned)__builtin_amdgcn_readfirstlane(vdst + (slot))); } while (0)
; template <class BIAS>
; __device__ __forceinline__ void attn_tiles(char* shm, const UnitIO& io, int t_begin, int t_end, const BIAS& B, int tid) {
;     ...
;         if (rem > 3) ATT_DMA(t + 3, ((t + 3 - t_begin) & 3) * SLOTB);
;         u32x4 pw[4]; f32x16 c1x;
;         if (act) {
;             bf16x8 kf[8]; const lds_cptr kp = kp0 + sl_c;
; #pragma unroll
;             for (int j = 0; j < 4; ++j) { kf[2 * j] = *(const __attribute__((address_space(3))) bf16x8*)(kp + j * 2048); kf[2 * j + 1] = *(const __attribute__((address_space(3))) bf16x8*)(kp + j * 2048 + 512); }
;             ATT_SBAR();
;             f32x16 c0, c1; B.init(c0, c1, t);
;             ATT_SBAR();
;             asm volatile("" : "+v"(kf[0]), "+v"(kf[1]), "+v"(kf[2]), "+v"(kf[3]), "+v"(kf[4]), "+v"(kf[5]), "+v"(kf[6]), "+v"(kf[7]));
; #pragma unroll
;             for (int d0 = 0; d0 < 4; ++d0) { c0 = __builtin_amdgcn_mfma_f32_32x32x16_bf16(kf[2 * d0], qr[d0], c0, 0, 0, 0); c1 = __builtin_amdgcn_mfma_f32_32x32x16_bf16(kf[2 * d0 + 1], qr[d0], c1, 0, 0, 0); }
.LBB0_303:
	s_waitcnt lgkmcnt(0)
	s_nop 0
	v_mfma_f32_32x32x16_bf16 v[50:65], v[98:101], v[66:69], v[50:65]
	v_mfma_f32_32x32x16_bf16 v[50:65], v[102:105], v[70:73], v[50:65]
	v_mfma_f32_32x32x16_bf16 v[50:65], v[106:109], v[74:77], v[50:65]
	v_mfma_f32_32x32x16_bf16 v[50:65], v[110:113], v[78:81], v[50:65]
	v_mfma_f32_32x32x16_bf16 v[34:49], v[94:97], v[66:69], v[34:49]
	s_and_b64 vcc, exec, s[12:13]
	s_cbranch_vccnz .Lmo_nodmaA
	s_cmp_eq_u32 s22, 0
	s_cselect_b32 s100, 0x6000, 0
	s_add_i32 s101, s100, s29
	s_mov_b32 m0, s101
	s_add_i32 s100, s100, s33
	global_load_lds_dwordx4 v[172:173], off
	s_mov_b32 m0, s100
	s_nop 0
	global_load_lds_dwordx4 v[152:153], off
	s_cmp_gt_u32 s28, 4
	s_cbranch_scc0 .Lmo_rq_a
	s_mov_b64 s[14:15], 0x20000
	v_lshl_add_u64 v[212:213], v[172:173], 0, s[14:15]
	v_lshl_add_u64 v[222:223], v[152:153], 0, s[14:15]
	s_cmp_eq_u32 s22, 0
	s_movk_i32 s100, 0x2000
	s_cselect_b32 s100, 0x1c000, s100
	s_add_i32 s101, s100, s29
	s_mov_b32 m0, s101
	s_add_i32 s100, s100, s33
	global_load_lds_dwordx4 v[212:213], off
	s_mov_b32 m0, s100
	s_nop 0
	global_load_lds_dwordx4 v[222:223], off
	s_cmp_gt_u32 s28, 5
	s_cbranch_scc0 .Lmo_rq_a
	v_lshl_add_u64 v[212:213], v[212:213], 0, s[14:15]
	v_lshl_add_u64 v[222:223], v[222:223], 0, s[14:15]
	s_cmp_eq_u32 s22, 0
	s_movk_i32 s100, 0x4000
	s_cselect_b32 s100, 0x1e000, s100
	s_add_i32 s101, s100, s29
	s_mov_b32 m0, s101
	s_add_i32 s100, s100, s33
	global_load_lds_dwordx4 v[212:213], off
	s_mov_b32 m0, s100
	s_nop 0
	global_load_lds_dwordx4 v[222:223], off
.Lmo_rq_a:
	s_nop 1
	s_branch .Lmo_go

; #define ATT_DMA(t, slot) do { glds16(ksrc + (long)(t) * tstep, (unsigned)__builtin_amdgcn_readfirstlane(kdst + (slot))); glds16(vsrc + (long)(t) * tstep, (unsigned)__builtin_amdgcn_readfirstlane(vdst + (slot))); } while (0)
; template <class BIAS>
; __device__ __forceinline__ void attn_tiles(char* shm, const UnitIO& io, int t_begin, int t_end, const BIAS& B, int tid) {
;     ...
;         const bool act = B.active(t);
;         const int sl_c = ((t - t_begin) & 3) * SLOTB;
;         if (rem > 3) ATT_DMA(t + 3, ((t + 3 - t_begin) & 3) * SLOTB);
;         u32x4 pw[4]; f32x16 c1x;
;         if (act) {
.Lmo_inact:
	s_and_b64 vcc, exec, s[12:13]
	s_cbranch_vccnz .Lmo_nodmaB
	s_cmp_eq_u32 s22, 0
	s_cselect_b32 s100, 0x6000, 0
	s_add_i32 s101, s100, s29
	s_mov_b32 m0, s101
	s_add_i32 s100, s100, s33
	global_load_lds_dwordx4 v[172:173], off
	s_mov_b32 m0, s100
	s_nop 0
	global_load_lds_dwordx4 v[152:153], off
	s_cmp_gt_u32 s28, 4
	s_cbranch_scc0 .Lmo_rq_b
	s_mov_b64 s[14:15], 0x20000
	v_lshl_add_u64 v[212:213], v[172:173], 0, s[14:15]
	v_lshl_add_u64 v[222:223], v[152:153], 0, s[14:15]
	s_cmp_eq_u32 s22, 0
	s_movk_i32 s100, 0x2000
	s_cselect_b32 s100, 0x1c000, s100
	s_add_i32 s101, s100, s29
	s_mov_b32 m0, s101
	s_add_i32 s100, s100, s33
	global_load_lds_dwordx4 v[212:213], off
	s_mov_b32 m0, s100
	s_nop 0
	global_load_lds_dwordx4 v[222:223], off
	s_cmp_gt_u32 s28, 5
	s_cbranch_scc0 .Lmo_rq_b
	v_lshl_add_u64 v[212:213], v[212:213], 0, s[14:15]
	v_lshl_add_u64 v[222:223], v[222:223], 0, s[14:15]
	s_cmp_eq_u32 s22, 0
	s_movk_i32 s100, 0x4000
	s_cselect_b32 s100, 0x1e000, s100
	s_add_i32 s101, s100, s29
	s_mov_b32 m0, s101
	s_add_i32 s100, s100, s33
	global_load_lds_dwordx4 v[212:213], off
	s_mov_b32 m0, s100
	s_nop 0
	global_load_lds_dwordx4 v[222:223], off
.Lmo_rq_b:
.Lmo_nodmaB:
	s_branch .Lmo_endstep

; #define ATT_WAIT_BAR(N) asm volatile("s_waitcnt vmcnt(" #N ") lgkmcnt(0)\n\ts_barrier" ::: "memory")
; template <class BIAS>
; __device__ __forceinline__ void attn_tiles(char* shm, const UnitIO& io, int t_begin, int t_end, const BIAS& B, int tid) {
;     ...
;         if (rem > 3) ATT_WAIT_BAR(4); else if (rem > 2) ATT_WAIT_BAR(2); else ATT_WAIT_BAR(0);
;     }
.Lmo_endstep:
	s_cmp_eq_u32 s28, 1
	s_cbranch_scc1 .Lmo_bar
	s_cmp_eq_u32 s22, 2
	s_cbranch_scc1 .Lmo_bar
	s_cmp_lg_u32 s22, 5
	s_cbranch_scc1 .LBB0_295
